# v16: v15 + NSA unit gate/slope parameter loads requested together with the q rows (one exposed round trip fewer per unit)
# baseline (speedup 1.0000x reference)
.LBB0_714:
	v_readlane_b32 s2, v254, 60
	s_min_i32 s2, s18, s2
	s_sub_i32 s2, s10, s2
	s_ashr_i32 s30, s2, 3
	s_ashr_i32 s68, s28, 6
	s_sub_i32 s65, 0x7f, s30
	s_waitcnt vmcnt(45)
	v_and_b32_e32 v191, 7, v184
	s_lshl_b32 s67, s68, 3
	s_bfe_u32 s26, s2, 0x20001
	s_and_b32 s71, s2, 1
	s_lshl_b32 s66, s65, 6
	v_or_b32_e32 v205, s67, v191
	v_readlane_b32 s2, v254, 62
	v_bfe_u32 v2, v184, 3, 2
	v_add_u32_e32 v185, s66, v205
	s_lshl_b32 s94, s26, 13
	v_readlane_b32 s3, v254, 63
	s_waitcnt vmcnt(22)
	v_lshl_or_b32 v8, s71, 2, v2
	v_add_u32_e32 v2, s94, v185
	v_mov_b64_e32 v[4:5], s[2:3]
	v_bfe_u32 v190, v184, 5, 1
	v_mad_i64_i32 v[4:5], s[2:3], v2, s76, v[4:5]
	v_lshlrev_b32_e32 v2, 8, v8
	v_lshl_add_u64 v[6:7], v[4:5], 0, v[2:3]
	v_lshlrev_b32_e32 v138, 4, v190
	v_mov_b32_e32 v139, v3
	v_lshl_add_u64 v[6:7], v[6:7], 0, v[138:139]
	global_load_dwordx4 v[10:13], v[6:7], off
	s_mov_b64 s[2:3], 0x2c00
	global_load_dwordx4 v[140:143], v[6:7], off offset:32
	global_load_dwordx4 v[144:147], v[6:7], off offset:64
	global_load_dwordx4 v[148:151], v[6:7], off offset:96
	global_load_dwordx4 v[152:155], v[6:7], off offset:128
	global_load_dwordx4 v[156:159], v[6:7], off offset:160
	global_load_dwordx4 v[160:163], v[6:7], off offset:192
	global_load_dwordx4 v[164:167], v[6:7], off offset:224
	v_mul_u32_u24_e32 v14, 3, v8
	v_lshlrev_b32_e32 v14, 1, v14
	v_mov_b32_e32 v15, v3
	v_lshl_add_u64 v[16:17], v[4:5], 0, v[14:15]
	v_lshl_add_u64 v[18:19], v[16:17], 0, s[2:3]
	v_add_co_u32_e32 v16, vcc, 0x2000, v16
	s_nop 1
	v_addc_co_u32_e32 v17, vcc, 0, v17, vcc
	global_load_dword v204, v[16:17], off offset:3072
	global_load_ushort v186, v[18:19], off offset:4
	s_waitcnt vmcnt(0)
	v_lshlrev_b32_e32 v2, 16, v10
	v_and_b32_e32 v9, 0xffff0000, v10
	v_mul_f32_e32 v2, 0x3e0293ee, v2
	v_mul_f32_e32 v9, 0x3e0293ee, v9
	v_cvt_pk_bf16_f32 v100, v2, v9
	v_lshlrev_b32_e32 v2, 16, v11
	v_and_b32_e32 v9, 0xffff0000, v11
	v_mul_f32_e32 v2, 0x3e0293ee, v2
	v_mul_f32_e32 v9, 0x3e0293ee, v9
	v_cvt_pk_bf16_f32 v101, v2, v9
	v_lshlrev_b32_e32 v2, 16, v12
	v_and_b32_e32 v9, 0xffff0000, v12
	v_mul_f32_e32 v2, 0x3e0293ee, v2
	v_mul_f32_e32 v9, 0x3e0293ee, v9
	v_cvt_pk_bf16_f32 v102, v2, v9
	v_lshlrev_b32_e32 v2, 16, v13
	v_and_b32_e32 v9, 0xffff0000, v13
	v_mul_f32_e32 v2, 0x3e0293ee, v2
	v_mul_f32_e32 v9, 0x3e0293ee, v9
	v_cvt_pk_bf16_f32 v103, v2, v9
	v_lshlrev_b32_e32 v2, 16, v140
	v_and_b32_e32 v9, 0xffff0000, v140
	v_mul_f32_e32 v2, 0x3e0293ee, v2
	v_mul_f32_e32 v9, 0x3e0293ee, v9
	v_cvt_pk_bf16_f32 v104, v2, v9
	v_lshlrev_b32_e32 v2, 16, v141
	v_and_b32_e32 v9, 0xffff0000, v141
	v_mul_f32_e32 v2, 0x3e0293ee, v2
	v_mul_f32_e32 v9, 0x3e0293ee, v9
	v_cvt_pk_bf16_f32 v105, v2, v9
	v_lshlrev_b32_e32 v2, 16, v142
	v_and_b32_e32 v9, 0xffff0000, v142
	v_mul_f32_e32 v2, 0x3e0293ee, v2
	v_mul_f32_e32 v9, 0x3e0293ee, v9
	v_cvt_pk_bf16_f32 v106, v2, v9
	v_lshlrev_b32_e32 v2, 16, v143
	v_and_b32_e32 v9, 0xffff0000, v143
	v_mul_f32_e32 v2, 0x3e0293ee, v2
	v_mul_f32_e32 v9, 0x3e0293ee, v9
	v_cvt_pk_bf16_f32 v107, v2, v9
	v_lshlrev_b32_e32 v2, 16, v144
	v_and_b32_e32 v9, 0xffff0000, v144
	v_mul_f32_e32 v2, 0x3e0293ee, v2
	v_mul_f32_e32 v9, 0x3e0293ee, v9
	v_cvt_pk_bf16_f32 v108, v2, v9
	v_lshlrev_b32_e32 v2, 16, v145
	v_and_b32_e32 v9, 0xffff0000, v145
	v_mul_f32_e32 v2, 0x3e0293ee, v2
	v_mul_f32_e32 v9, 0x3e0293ee, v9
	v_cvt_pk_bf16_f32 v109, v2, v9
	v_lshlrev_b32_e32 v2, 16, v146
	v_and_b32_e32 v9, 0xffff0000, v146
	v_mul_f32_e32 v2, 0x3e0293ee, v2
	v_mul_f32_e32 v9, 0x3e0293ee, v9
	v_cvt_pk_bf16_f32 v110, v2, v9
	v_lshlrev_b32_e32 v2, 16, v147
	v_and_b32_e32 v9, 0xffff0000, v147
	v_mul_f32_e32 v2, 0x3e0293ee, v2
	v_mul_f32_e32 v9, 0x3e0293ee, v9
	v_cvt_pk_bf16_f32 v111, v2, v9
	v_lshlrev_b32_e32 v2, 16, v148
	v_and_b32_e32 v9, 0xffff0000, v148
	v_mul_f32_e32 v2, 0x3e0293ee, v2
	v_mul_f32_e32 v9, 0x3e0293ee, v9
	v_cvt_pk_bf16_f32 v112, v2, v9
	v_lshlrev_b32_e32 v2, 16, v149
	v_and_b32_e32 v9, 0xffff0000, v149
	v_mul_f32_e32 v2, 0x3e0293ee, v2
	v_mul_f32_e32 v9, 0x3e0293ee, v9
	v_cvt_pk_bf16_f32 v113, v2, v9
	v_lshlrev_b32_e32 v2, 16, v150
	v_and_b32_e32 v9, 0xffff0000, v150
	v_mul_f32_e32 v2, 0x3e0293ee, v2
	v_mul_f32_e32 v9, 0x3e0293ee, v9
	v_cvt_pk_bf16_f32 v114, v2, v9
	v_lshlrev_b32_e32 v2, 16, v151
	v_and_b32_e32 v9, 0xffff0000, v151
	v_mul_f32_e32 v2, 0x3e0293ee, v2
	v_mul_f32_e32 v9, 0x3e0293ee, v9
	v_cvt_pk_bf16_f32 v115, v2, v9
	v_lshlrev_b32_e32 v2, 16, v152
	v_and_b32_e32 v9, 0xffff0000, v152
	v_mul_f32_e32 v2, 0x3e0293ee, v2
	v_mul_f32_e32 v9, 0x3e0293ee, v9
	v_cvt_pk_bf16_f32 v116, v2, v9
	v_lshlrev_b32_e32 v2, 16, v153
	v_and_b32_e32 v9, 0xffff0000, v153
	v_mul_f32_e32 v2, 0x3e0293ee, v2
	v_mul_f32_e32 v9, 0x3e0293ee, v9
	v_cvt_pk_bf16_f32 v117, v2, v9
	v_lshlrev_b32_e32 v2, 16, v154
	v_and_b32_e32 v9, 0xffff0000, v154
	v_mul_f32_e32 v2, 0x3e0293ee, v2
	v_mul_f32_e32 v9, 0x3e0293ee, v9
	v_cvt_pk_bf16_f32 v118, v2, v9
	v_lshlrev_b32_e32 v2, 16, v155
	v_and_b32_e32 v9, 0xffff0000, v155
	v_mul_f32_e32 v2, 0x3e0293ee, v2
	v_mul_f32_e32 v9, 0x3e0293ee, v9
	v_cvt_pk_bf16_f32 v119, v2, v9
	v_lshlrev_b32_e32 v2, 16, v156
	v_and_b32_e32 v9, 0xffff0000, v156
	v_mul_f32_e32 v2, 0x3e0293ee, v2
	v_mul_f32_e32 v9, 0x3e0293ee, v9
	v_cvt_pk_bf16_f32 v120, v2, v9
	v_lshlrev_b32_e32 v2, 16, v157
	v_and_b32_e32 v9, 0xffff0000, v157
	v_mul_f32_e32 v2, 0x3e0293ee, v2
	v_mul_f32_e32 v9, 0x3e0293ee, v9
	v_cvt_pk_bf16_f32 v121, v2, v9
	v_lshlrev_b32_e32 v2, 16, v158
	v_and_b32_e32 v9, 0xffff0000, v158
	v_mul_f32_e32 v2, 0x3e0293ee, v2
	v_mul_f32_e32 v9, 0x3e0293ee, v9
	v_cvt_pk_bf16_f32 v122, v2, v9
	v_lshlrev_b32_e32 v2, 16, v159
	v_and_b32_e32 v9, 0xffff0000, v159
	v_mul_f32_e32 v2, 0x3e0293ee, v2
	v_mul_f32_e32 v9, 0x3e0293ee, v9
	v_cvt_pk_bf16_f32 v123, v2, v9
	v_lshlrev_b32_e32 v2, 16, v160
	v_and_b32_e32 v9, 0xffff0000, v160
	v_mul_f32_e32 v2, 0x3e0293ee, v2
	v_mul_f32_e32 v9, 0x3e0293ee, v9
	v_cvt_pk_bf16_f32 v124, v2, v9
	v_lshlrev_b32_e32 v2, 16, v161
	v_and_b32_e32 v9, 0xffff0000, v161
	v_mul_f32_e32 v2, 0x3e0293ee, v2
	v_mul_f32_e32 v9, 0x3e0293ee, v9
	v_cvt_pk_bf16_f32 v125, v2, v9
	v_lshlrev_b32_e32 v2, 16, v162
	v_and_b32_e32 v9, 0xffff0000, v162
	v_mul_f32_e32 v2, 0x3e0293ee, v2
	v_mul_f32_e32 v9, 0x3e0293ee, v9
	v_cvt_pk_bf16_f32 v126, v2, v9
	v_lshlrev_b32_e32 v2, 16, v163
	v_and_b32_e32 v9, 0xffff0000, v163
	v_mul_f32_e32 v2, 0x3e0293ee, v2
	v_mul_f32_e32 v9, 0x3e0293ee, v9
	v_cvt_pk_bf16_f32 v127, v2, v9
	v_lshlrev_b32_e32 v2, 16, v164
	v_mul_f32_e32 v2, 0x3e0293ee, v2
	v_and_b32_e32 v6, 0xffff0000, v164
	v_mul_f32_e32 v6, 0x3e0293ee, v6
	v_cvt_pk_bf16_f32 v128, v2, v6
	v_lshlrev_b32_e32 v2, 16, v165
	v_mul_f32_e32 v2, 0x3e0293ee, v2
	v_and_b32_e32 v6, 0xffff0000, v165
	v_mul_f32_e32 v6, 0x3e0293ee, v6
	v_cvt_pk_bf16_f32 v129, v2, v6
	v_lshlrev_b32_e32 v2, 16, v166
	v_mul_f32_e32 v2, 0x3e0293ee, v2
	v_and_b32_e32 v6, 0xffff0000, v166
	v_mul_f32_e32 v6, 0x3e0293ee, v6
	v_cvt_pk_bf16_f32 v130, v2, v6
	v_lshlrev_b32_e32 v2, 16, v167
	v_mul_f32_e32 v2, 0x3e0293ee, v2
	v_and_b32_e32 v6, 0xffff0000, v167
	v_mul_f32_e32 v6, 0x3e0293ee, v6
	v_cvt_pk_bf16_f32 v131, v2, v6
	s_movk_i32 s2, 0x2100
	v_cmp_gt_i32_e32 vcc, s2, v184
	s_and_saveexec_b64 s[2:3], vcc
	s_cbranch_execz .LBB0_717
	v_readlane_b32 s6, v255, 10
	v_add_u32_e32 v2, 0xfffffe00, v184
	s_nop 0
	v_lshl_add_u32 v4, v184, 2, s6
	s_mov_b64 s[6:7], 0
